# best + sub-microsecond per-CU skew at P10 start (B-tile sharers desynchronized)
# speedup vs baseline: 1.0129x; 1.0129x over previous
;     __device__ __forceinline__ bool next(int i, pg8::Unit& u) const { const int s = i >= R ? 1 : 0; const bool ok = so.next(i - s * R, u); u.sel = s; return ok && i < 2 * R; }
; template <class Epi, class Sched>
; __device__ __forceinline__ void gemm_phase_gather(PG8_LAS unsigned char* lds, const Gemm g, const int* __restrict__ gidx, PG8_LAS int* itab  , const Sched& S, const Epi& E) {
;     ...
;     { int vals[4];
; #pragma unroll
;       for (int k = 0; k < 4; ++k) { const int e = tid + 512 * k; Unit uu; const bool ok = S.next(e >> 8, uu); vals[k] = ok ? gidx[uu.pm * BM + (e & 255)] : 0; }
;     __device__ __forceinline__ bool next(int i, pg8::Unit& u) const {
;         constexpr int NWG = NE * 8 * NJ, Q = NWG / 8;
;         const int L = i * G + c; if (L >= NWG) return false;
;         const int wgid = (L % 8) * Q + L / 8;
;         const int e = wgid / (8 * NJ), w = wgid % (8 * NJ), rt = w % 8, j = w / 8, b = rt >> 1, half = rt & 1;
;         u.pm = (b * NE + e) * 2 + half; u.pn = e * NJ + j; return true;
.LBB0_1258:
	s_cmp_lt_i32 s78, 11
	s_cselect_b64 s[0:1], -1, 0
	s_cmp_gt_i32 s79, 10
	s_cselect_b64 s[2:3], -1, 0
	s_and_b64 s[0:1], s[0:1], s[2:3]
	s_andn2_b64 vcc, exec, s[0:1]
	s_cbranch_vccnz .LBB0_1339
	s_lshr_b32 s100, s88, 3
	s_and_b32 s100, s100, 7
	s_cmp_eq_u32 s100, 0
	s_cbranch_scc1 .Lskew10_done
.Lskew10_loop:
	s_sleep 5
	s_sub_u32 s100, s100, 1
	s_cmp_lg_u32 s100, 0
	s_cbranch_scc1 .Lskew10_loop
.Lskew10_done:
	s_mov_b64 s[0:1], s[74:75]
	s_load_dwordx2 s[0:1], s[0:1], 0xd8
	v_lshrrev_b32_e32 v2, 8, v0
	v_mul_lo_u32 v2, s86, v2
	v_add_u32_e32 v4, s88, v2
	s_movk_i32 s7, 0x800
	s_waitcnt lgkmcnt(0)
	s_add_u32 s2, s0, 0x400000
	v_readfirstlane_b32 s6, v0
	v_and_b32_e32 v1, 0xff, v0
	s_addc_u32 s3, s1, 0
	v_cmp_gt_i32_e32 vcc, s7, v4
	v_mov_b32_e32 v2, 0
	v_mov_b32_e32 v3, 0
	s_and_saveexec_b64 s[4:5], vcc
	s_cbranch_execz .LBB0_1261
	v_ashrrev_i32_e32 v3, 31, v4
	v_lshrrev_b32_e32 v3, 29, v3
	v_add_u32_e32 v3, v4, v3
	v_ashrrev_i32_e32 v5, 3, v3
	v_and_b32_e32 v3, 0xfffff8, v3
	v_sub_u32_e32 v3, v4, v3
	v_lshl_add_u32 v3, v3, 8, v5
	v_ashrrev_i32_e32 v5, 31, v3
	v_lshrrev_b32_e32 v5, 25, v5
	v_add_u32_e32 v5, v3, v5
	v_lshrrev_b32_e32 v6, 7, v5
	v_and_b32_e32 v5, 0xff80, v5
	v_sub_u32_e32 v3, v3, v5
	v_mov_b32_e32 v5, 12
	v_lshrrev_b16_sdwa v5, v5, sext(v3) dst_sel:DWORD dst_unused:UNUSED_PAD src0_sel:DWORD src1_sel:BYTE_0
	v_and_b32_e32 v5, 7, v5
	v_add_u16_e32 v5, v3, v5
	v_and_b32_e32 v5, 0xf8, v5
	v_sub_u16_e32 v3, v3, v5
	v_mov_b32_e32 v5, 3
	v_lshlrev_b32_sdwa v5, v5, sext(v3) dst_sel:DWORD dst_unused:UNUSED_PAD src0_sel:DWORD src1_sel:BYTE_0
	v_and_b32_e32 v5, 0x7ffff0, v5
	v_lshlrev_b32_e32 v3, 8, v3
	v_add_lshl_u32 v5, v5, v6, 9
	v_and_b32_e32 v3, 0x100, v3
	v_or3_b32 v6, v5, v3, v1
	v_ashrrev_i32_e32 v7, 31, v6
	v_lshl_add_u64 v[6:7], v[6:7], 2, s[2:3]
	global_load_dword v3, v[6:7], off
